# GLA units: the low-rank gate row load (and its address arithmetic) issued with the unit's q/k/v loads before the first workgroup barrier instead of behind it
# baseline (speedup 1.0000x reference)
.LBB0_759:
	s_waitcnt vmcnt(3)
	v_ashrrev_i32_e32 v18, 3, v39
	v_ashrrev_i32_e32 v19, 31, v18
	s_waitcnt vmcnt(0)
	v_lshl_add_u64 v[2:3], s[22:23], 0, v[18:19]
	v_mad_u64_u32 v[4:5], s[4:5], v2, s27, v[16:17]
	v_mov_b32_e32 v2, v5
	s_and_b32 s55, s54, 3
	v_mad_u64_u32 v[2:3], s[4:5], v3, s27, v[2:3]
	v_and_b32_e32 v38, 7, v39
	v_mov_b32_e32 v5, v2
	s_lshl_b32 s16, s55, 7
	v_lshl_add_u64 v[2:3], v[4:5], 0, s[16:17]
	v_lshlrev_b32_e32 v14, 4, v38
	v_lshl_add_u64 v[2:3], v[2:3], 0, v[14:15]
	v_add_co_u32_e32 v20, vcc, s28, v2
	s_lshl_b32 s16, s55, 8
	s_nop 0
	v_addc_co_u32_e32 v21, vcc, 0, v3, vcc
	v_lshl_add_u64 v[2:3], v[4:5], 0, s[16:17]
	v_lshlrev_b32_e32 v14, 5, v38
	v_lshl_add_u64 v[2:3], v[2:3], 0, v[14:15]
	v_add_co_u32_e32 v24, vcc, 0x1000, v2
	v_lshl_add_u64 v[22:23], v[2:3], 0, s[18:19]
	s_nop 0
	v_addc_co_u32_e32 v25, vcc, 0, v3, vcc
	global_load_dwordx4 v[6:9], v[24:25], off offset:1536
	global_load_dwordx4 v[10:13], v[20:21], off offset:1024
	global_load_dwordx4 v[2:5], v[22:23], off offset:16
	v_cmp_gt_i32_e32 vcc, s29, v39
	s_and_saveexec_b64 s[24:25], vcc
	s_cbranch_execz .Lglr_pre0
	v_ashrrev_i32_e32 v24, 2, v39
	v_ashrrev_i32_e32 v25, 31, v24
	v_lshl_add_u64 v[20:21], s[22:23], 0, v[24:25]
	v_mad_u64_u32 v[22:23], s[22:23], v20, s27, v[16:17]
	v_mov_b32_e32 v14, v23
	v_mad_u64_u32 v[20:21], s[22:23], v21, s27, v[14:15]
	v_lshlrev_b32_e32 v14, 3, v39
	v_and_b32_e32 v19, 24, v14
	v_mov_b32_e32 v23, v20
	v_lshlrev_b32_e32 v14, 1, v19
	v_lshl_add_u64 v[20:21], v[22:23], 0, v[14:15]
	v_add_co_u32_e32 v20, vcc, s28, v20
	v_lshlrev_b32_e32 v14, 7, v24
	s_nop 0
	v_addc_co_u32_e32 v21, vcc, 0, v21, vcc
	global_load_dwordx4 v[20:23], v[20:21], off offset:3584
	v_lshlrev_b32_e32 v19, 2, v19
	v_add3_u32 v14, 0, v14, v19
.Lglr_pre0:
	s_or_b64 exec, exec, s[24:25]
	s_barrier
	s_load_dwordx4 s[4:7], s[0:1], 0x88
	v_cmp_gt_i32_e32 vcc, s29, v39
	s_and_saveexec_b64 s[24:25], vcc
	s_cbranch_execz .LBB0_761
	s_waitcnt vmcnt(0)
	v_lshlrev_b32_e32 v24, 16, v20
	v_and_b32_e32 v25, 0xffff0000, v20
	v_lshlrev_b32_e32 v26, 16, v21
	v_and_b32_e32 v27, 0xffff0000, v21
	v_lshlrev_b32_e32 v20, 16, v22
	v_and_b32_e32 v21, 0xffff0000, v22
	v_lshlrev_b32_e32 v22, 16, v23
	v_and_b32_e32 v23, 0xffff0000, v23
	ds_write_b128 v14, v[24:27] offset:32768
	ds_write_b128 v14, v[20:23] offset:32784

.LBB0_1360:
	s_or_b64 exec, exec, s[4:5]
	s_add_i32 s4, s85, 0xfffffce0
	s_mul_hi_i32 s5, s4, 0x3e0f83e1
	s_lshr_b32 s6, s5, 31
	s_ashr_i32 s67, s5, 5
	s_add_i32 s67, s67, s6
	s_mul_i32 s5, s67, 0x84
	s_sub_i32 s68, s4, s5
	s_ashr_i32 s4, s67, 2
	s_and_b32 s34, s67, 3
	s_cmp_lt_i32 s68, 4
	s_cselect_b64 s[6:7], -1, 0
	s_cmp_gt_i32 s68, 3
	s_cselect_b64 s[28:29], -1, 0
	s_ashr_i32 s5, s4, 31
	s_lshl_b32 s26, s4, 8
	s_lshl_b32 s14, s68, 6
	s_lshl_b64 s[24:25], s[4:5], 13
	s_ashr_i32 s27, s26, 31
	s_and_b64 s[4:5], s[6:7], exec
	s_cselect_b32 s4, s38, 0xffffff00
	s_cselect_b32 s5, s27, s25
	s_cselect_b32 s6, s26, s24
	s_add_i32 s4, s4, s14
	v_mov_b32 v87, v0
	s_add_u32 s26, s6, s4
	s_waitcnt vmcnt(3)
	v_ashrrev_i32_e32 v18, 3, v87
	s_addc_u32 s27, s5, 0
	v_ashrrev_i32_e32 v19, 31, v18
	s_waitcnt vmcnt(0)
	v_lshl_add_u64 v[2:3], s[26:27], 0, v[18:19]
	v_mad_u64_u32 v[4:5], s[4:5], v2, s39, v[76:77]
	v_and_b32_e32 v36, 7, v87
	v_mad_i32_i24 v5, v3, s39, v5
	s_lshl_b32 s14, s34, 7
	v_lshlrev_b32_e32 v74, 4, v36
	v_lshl_add_u64 v[2:3], v[4:5], 0, s[14:15]
	v_lshl_add_u64 v[2:3], v[2:3], 0, v[74:75]
	v_add_co_u32_e32 v2, vcc, s50, v2
	s_lshl_b32 s4, s34, 8
	s_nop 0
	v_addc_co_u32_e32 v3, vcc, 0, v3, vcc
	s_mov_b32 s5, s15
	global_load_dwordx4 v[14:17], v[2:3], off offset:512
	global_load_dwordx4 v[10:13], v[2:3], off offset:1024
	v_lshl_add_u64 v[2:3], v[4:5], 0, s[4:5]
	v_lshlrev_b32_e32 v74, 5, v36
	v_lshl_add_u64 v[2:3], v[2:3], 0, v[74:75]
	v_lshl_add_u64 v[4:5], v[2:3], 0, s[16:17]
	v_add_co_u32_e32 v2, vcc, 0x1000, v2
	v_readfirstlane_b32 s69, v87
	s_nop 0
	v_addc_co_u32_e32 v3, vcc, 0, v3, vcc
	global_load_dwordx4 v[6:9], v[2:3], off offset:1536
	s_nop 0
	global_load_dwordx4 v[2:5], v[4:5], off offset:16
	v_cmp_gt_i32_e32 vcc, s51, v87
	s_and_saveexec_b64 s[30:31], vcc
	s_cbranch_execz .Lglr_pre1
	v_ashrrev_i32_e32 v24, 2, v87
	v_ashrrev_i32_e32 v25, 31, v24
	v_lshl_add_u64 v[20:21], s[26:27], 0, v[24:25]
	v_mad_u64_u32 v[22:23], s[70:71], v20, s39, v[76:77]
	v_mov_b32_e32 v20, v23
	v_lshlrev_b32_e32 v19, 3, v87
	v_mad_u64_u32 v[20:21], s[70:71], v21, s39, v[20:21]
	v_and_b32_e32 v19, 24, v19
	v_mov_b32_e32 v23, v20
	v_lshlrev_b32_e32 v74, 1, v19
	v_lshl_add_u64 v[20:21], v[22:23], 0, v[74:75]
	v_add_co_u32_e32 v20, vcc, s50, v20
	v_lshlrev_b32_e32 v24, 7, v24
	s_nop 0
	v_addc_co_u32_e32 v21, vcc, 0, v21, vcc
	global_load_dwordx4 v[20:23], v[20:21], off offset:3584
	v_lshlrev_b32_e32 v19, 2, v19
	v_add3_u32 v19, 0, v24, v19
.Lglr_pre1:
	s_or_b64 exec, exec, s[30:31]
	s_load_dwordx4 s[4:7], s[0:1], 0x88
	s_load_dwordx2 s[24:25], s[0:1], 0x98
	v_cmp_gt_i32_e32 vcc, s51, v87
	s_waitcnt lgkmcnt(0)
	s_barrier
	s_and_saveexec_b64 s[30:31], vcc
	s_cbranch_execz .LBB0_1362
	s_waitcnt vmcnt(0)
	v_lshlrev_b32_e32 v24, 16, v20
	v_and_b32_e32 v25, 0xffff0000, v20
	v_lshlrev_b32_e32 v26, 16, v21
	v_and_b32_e32 v27, 0xffff0000, v21
	v_lshlrev_b32_e32 v20, 16, v22
	v_and_b32_e32 v21, 0xffff0000, v22
	v_lshlrev_b32_e32 v22, 16, v23
	v_and_b32_e32 v23, 0xffff0000, v23
	ds_write_b128 v19, v[24:27] offset:32768
	ds_write_b128 v19, v[20:23] offset:32784

.LBB0_2485:
	v_ashrrev_i32_e32 v18, 3, v39
	v_ashrrev_i32_e32 v19, 31, v18
	v_lshl_add_u64 v[2:3], s[24:25], 0, v[18:19]
	v_mad_u64_u32 v[4:5], s[4:5], v2, s29, v[16:17]
	v_mov_b32_e32 v2, v5
	s_and_b32 s60, s59, 3
	v_mad_u64_u32 v[2:3], s[4:5], v3, s29, v[2:3]
	v_and_b32_e32 v38, 7, v39
	v_mov_b32_e32 v5, v2
	s_lshl_b32 s16, s60, 7
	v_lshl_add_u64 v[2:3], v[4:5], 0, s[16:17]
	v_lshlrev_b32_e32 v14, 4, v38
	v_lshl_add_u64 v[2:3], v[2:3], 0, v[14:15]
	s_lshl_b32 s16, s60, 8
	v_add_co_u32_e32 v2, vcc, s30, v2
	v_lshl_add_u64 v[4:5], v[4:5], 0, s[16:17]
	v_lshlrev_b32_e32 v14, 5, v38
	v_addc_co_u32_e32 v3, vcc, 0, v3, vcc
	v_lshl_add_u64 v[4:5], v[4:5], 0, v[14:15]
	v_lshl_add_u64 v[20:21], v[4:5], 0, s[18:19]
	v_add_co_u32_e32 v4, vcc, 0x1000, v4
	s_nop 1
	v_addc_co_u32_e32 v5, vcc, 0, v5, vcc
	global_load_dwordx4 v[6:9], v[4:5], off offset:1536
	global_load_dwordx4 v[10:13], v[2:3], off offset:1024
	s_nop 0
	global_load_dwordx4 v[2:5], v[20:21], off offset:16
	v_cmp_gt_i32_e32 vcc, s31, v39
	s_and_saveexec_b64 s[26:27], vcc
	s_cbranch_execz .Lglr_pre2
	v_ashrrev_i32_e32 v24, 2, v39
	v_ashrrev_i32_e32 v25, 31, v24
	v_lshl_add_u64 v[20:21], s[24:25], 0, v[24:25]
	v_mad_u64_u32 v[22:23], s[24:25], v20, s29, v[16:17]
	v_mov_b32_e32 v14, v23
	v_mad_u64_u32 v[20:21], s[24:25], v21, s29, v[14:15]
	v_lshlrev_b32_e32 v14, 3, v39
	v_and_b32_e32 v19, 24, v14
	v_mov_b32_e32 v23, v20
	v_lshlrev_b32_e32 v14, 1, v19
	v_lshl_add_u64 v[20:21], v[22:23], 0, v[14:15]
	v_add_co_u32_e32 v20, vcc, s30, v20
	v_lshlrev_b32_e32 v14, 7, v24
	s_nop 0
	v_addc_co_u32_e32 v21, vcc, 0, v21, vcc
	global_load_dwordx4 v[20:23], v[20:21], off offset:3584
	v_lshlrev_b32_e32 v19, 2, v19
	v_add3_u32 v14, 0, v14, v19
.Lglr_pre2:
	s_or_b64 exec, exec, s[26:27]
	s_barrier
	s_load_dwordx4 s[4:7], s[0:1], 0x88
	v_cmp_gt_i32_e32 vcc, s31, v39
	s_and_saveexec_b64 s[26:27], vcc
	s_cbranch_execz .LBB0_2487
	s_waitcnt vmcnt(0)
	v_lshlrev_b32_e32 v24, 16, v20
	v_and_b32_e32 v25, 0xffff0000, v20
	v_lshlrev_b32_e32 v26, 16, v21
	v_and_b32_e32 v27, 0xffff0000, v21
	v_lshlrev_b32_e32 v20, 16, v22
	v_and_b32_e32 v21, 0xffff0000, v22
	v_lshlrev_b32_e32 v22, 16, v23
	v_and_b32_e32 v23, 0xffff0000, v23
	ds_write_b128 v14, v[24:27] offset:32768
	ds_write_b128 v14, v[20:23] offset:32784

.LBB0_2875:
	s_or_b64 exec, exec, s[4:5]
	s_add_i32 s4, s85, 0xfffffd00
	s_ashr_i32 s5, s4, 31
	s_lshr_b32 s5, s5, 25
	s_add_i32 s5, s4, s5
	s_and_b32 s6, s5, 0xffffff80
	s_ashr_i32 s72, s5, 7
	s_sub_i32 s74, s4, s6
	s_add_i32 s73, s74, 4
	s_ashr_i32 s4, s5, 9
	s_and_b32 s38, s72, 3
	s_cmp_lt_i32 s74, 0
	s_cselect_b64 s[6:7], -1, 0
	s_cmp_gt_i32 s74, -1
	s_cselect_b64 s[30:31], -1, 0
	s_ashr_i32 s5, s4, 31
	s_lshl_b32 s28, s4, 8
	s_lshl_b32 s14, s73, 6
	s_lshl_b64 s[26:27], s[4:5], 13
	s_ashr_i32 s29, s28, 31
	s_and_b64 s[4:5], s[6:7], exec
	s_cselect_b32 s4, s50, 0xffffff00
	s_cselect_b32 s5, s29, s27
	s_cselect_b32 s6, s28, s26
	s_add_i32 s14, s14, s4
	v_mov_b32 v87, v0
	s_add_u32 s28, s6, s14
	v_ashrrev_i32_e32 v18, 3, v87
	s_addc_u32 s29, s5, 0
	v_ashrrev_i32_e32 v19, 31, v18
	v_lshl_add_u64 v[2:3], s[28:29], 0, v[18:19]
	v_mad_u64_u32 v[4:5], s[4:5], v2, s51, v[76:77]
	v_and_b32_e32 v36, 7, v87
	v_mad_i32_i24 v5, v3, s51, v5
	s_lshl_b32 s14, s38, 7
	v_lshlrev_b32_e32 v74, 4, v36
	v_lshl_add_u64 v[2:3], v[4:5], 0, s[14:15]
	v_lshl_add_u64 v[2:3], v[2:3], 0, v[74:75]
	v_add_co_u32_e32 v2, vcc, s52, v2
	s_lshl_b32 s4, s38, 8
	s_nop 0
	v_addc_co_u32_e32 v3, vcc, 0, v3, vcc
	s_mov_b32 s5, s15
	global_load_dwordx4 v[14:17], v[2:3], off offset:512
	global_load_dwordx4 v[10:13], v[2:3], off offset:1024
	v_lshl_add_u64 v[2:3], v[4:5], 0, s[4:5]
	v_lshlrev_b32_e32 v74, 5, v36
	v_lshl_add_u64 v[2:3], v[2:3], 0, v[74:75]
	v_lshl_add_u64 v[4:5], v[2:3], 0, s[16:17]
	v_add_co_u32_e32 v2, vcc, 0x1000, v2
	v_readfirstlane_b32 s75, v87
	s_nop 0
	v_addc_co_u32_e32 v3, vcc, 0, v3, vcc
	global_load_dwordx4 v[6:9], v[2:3], off offset:1536
	s_nop 0
	global_load_dwordx4 v[2:5], v[4:5], off offset:16
	v_cmp_gt_i32_e32 vcc, s53, v87
	s_and_saveexec_b64 s[34:35], vcc
	s_cbranch_execz .Lglr_pre3
	v_ashrrev_i32_e32 v24, 2, v87
	v_ashrrev_i32_e32 v25, 31, v24
	v_lshl_add_u64 v[20:21], s[28:29], 0, v[24:25]
	v_mad_u64_u32 v[22:23], s[76:77], v20, s51, v[76:77]
	v_mov_b32_e32 v20, v23
	v_lshlrev_b32_e32 v19, 3, v87
	v_mad_u64_u32 v[20:21], s[76:77], v21, s51, v[20:21]
	v_and_b32_e32 v19, 24, v19
	v_mov_b32_e32 v23, v20
	v_lshlrev_b32_e32 v74, 1, v19
	v_lshl_add_u64 v[20:21], v[22:23], 0, v[74:75]
	v_add_co_u32_e32 v20, vcc, s52, v20
	v_lshlrev_b32_e32 v24, 7, v24
	s_nop 0
	v_addc_co_u32_e32 v21, vcc, 0, v21, vcc
	global_load_dwordx4 v[20:23], v[20:21], off offset:3584
	v_lshlrev_b32_e32 v19, 2, v19
	v_add3_u32 v19, 0, v24, v19
.Lglr_pre3:
	s_or_b64 exec, exec, s[34:35]
	s_load_dwordx4 s[4:7], s[0:1], 0x88
	s_load_dwordx2 s[26:27], s[0:1], 0x98
	v_cmp_gt_i32_e32 vcc, s53, v87
	s_waitcnt lgkmcnt(0)
	s_barrier
	s_and_saveexec_b64 s[34:35], vcc
	s_cbranch_execz .LBB0_2877
	s_waitcnt vmcnt(0)
	v_lshlrev_b32_e32 v24, 16, v20
	v_and_b32_e32 v25, 0xffff0000, v20
	v_lshlrev_b32_e32 v26, 16, v21
	v_and_b32_e32 v27, 0xffff0000, v21
	v_lshlrev_b32_e32 v20, 16, v22
	v_and_b32_e32 v21, 0xffff0000, v22
	v_lshlrev_b32_e32 v22, 16, v23
	v_and_b32_e32 v23, 0xffff0000, v23
	ds_write_b128 v19, v[24:27] offset:32768
	ds_write_b128 v19, v[20:23] offset:32784
